# baseline (speedup 1.0000x reference)
.Ltg2_go:
	s_nop 1
	v_accvgpr_read_b32 v30, a128
	v_accvgpr_read_b32 v32, a129
	v_accvgpr_read_b32 v31, a130
	v_accvgpr_read_b32 v33, a131
	v_cvt_pk_f16_f32 v31, v31, v33
	v_cvt_pk_f16_f32 v30, v30, v32
	v_accvgpr_read_b32 v32, a132
	v_accvgpr_read_b32 v34, a133
	v_accvgpr_read_b32 v33, a134
	v_accvgpr_read_b32 v35, a135
	v_cvt_pk_f16_f32 v33, v33, v35
	v_cvt_pk_f16_f32 v32, v32, v34
	ds_write2_b64 v221, v[30:31], v[32:33] offset0:32 offset1:64
	s_waitcnt lgkmcnt(0)
	s_barrier
	ds_read_b128 v[34:37], v249
	ds_read_b128 v[38:41], v249 offset:64
	ds_read_b128 v[42:45], v249 offset:256
	ds_read_b128 v[46:49], v249 offset:320
	ds_read_b128 v[50:53], v249 offset:512
	ds_read_b128 v[30:33], v249 offset:576
	ds_read2st64_b32 v[56:57], v184 offset0:100 offset1:101
	ds_read2st64_b32 v[54:55], v184 offset0:102 offset1:103
	s_waitcnt lgkmcnt(7)
	v_mfma_f32_16x16x32_f16 a[4:7], v[34:37], v[0:3], a[4:7]
	s_waitcnt lgkmcnt(6)
	v_mfma_f32_16x16x32_f16 a[4:7], v[38:41], v[64:67], a[4:7]
	s_waitcnt lgkmcnt(5)
	v_mfma_f32_16x16x32_f16 a[4:7], v[42:45], v[68:71], a[4:7]
	s_waitcnt lgkmcnt(4)
	v_mfma_f32_16x16x32_f16 a[4:7], v[46:49], v[72:75], a[4:7]
	s_waitcnt lgkmcnt(3)
	v_mfma_f32_16x16x32_f16 a[4:7], v[50:53], v[78:81], a[4:7]
	s_waitcnt lgkmcnt(2)
	v_mfma_f32_16x16x32_f16 a[4:7], v[30:33], v[82:85], a[4:7]
	s_waitcnt vmcnt(0)
	s_nop 7
	v_accvgpr_read_b32 v0, a4
	v_accvgpr_read_b32 v1, a5
	v_accvgpr_read_b32 v2, a6
	v_accvgpr_read_b32 v3, a7
	v_add_f32_e32 v0, v180, v0
	v_add_f32_e32 v1, v180, v1
	v_add_f32_e32 v2, v180, v2
	v_add_f32_e32 v3, v180, v3
	v_mul_f32_e32 v0, 0xbfb8aa3b, v0
	v_mul_f32_e32 v1, 0xbfb8aa3b, v1
	v_mul_f32_e32 v2, 0xbfb8aa3b, v2
	v_mul_f32_e32 v3, 0xbfb8aa3b, v3
	v_exp_f32_e32 v0, v0
	v_exp_f32_e32 v1, v1
	v_exp_f32_e32 v2, v2
	v_exp_f32_e32 v3, v3
	v_add_f32_e32 v0, 1.0, v0
	v_add_f32_e32 v1, 1.0, v1
	v_add_f32_e32 v2, 1.0, v2
	v_add_f32_e32 v3, 1.0, v3
	v_rcp_f32_e32 v186, v0
	v_rcp_f32_e32 v252, v1
	v_rcp_f32_e32 v253, v2
	v_rcp_f32_e32 v254, v3
	s_waitcnt lgkmcnt(0)
	s_and_b64 vcc, exec, s[16:17]
	v_mul_f32_e32 v0, v56, v186
	v_mul_f32_e32 v1, v57, v252
	v_mul_f32_e32 v2, v54, v253
	v_mul_f32_e32 v3, v55, v254
	v_cvt_pk_f16_f32 v180, v0, v1
	v_cvt_pk_f16_f32 v181, v2, v3
	s_cbranch_vccnz .LBB1_143
	global_store_dwordx2 v[172:173], v[180:181], off
	s_or_b32 s70, s40, 3
	s_and_saveexec_b64 s[68:69], s[12:13]
	v_mov_b32_e32 v3, s70
	global_store_dword v[174:175], v3, off
	s_mov_b64 exec, s[68:69]
	s_mov_b64 s[36:37], 0
